# barrier acquire: every workgroup issues its agent-scope buffer_inv sc1 right after arriving (no cached loads are issued between arrival and release: other waves are parked at s_barrier, polls are sc1)
# baseline (speedup 1.0000x reference)
; template <class T> __device__ __forceinline__ T* opaque_p(T* p) { asm volatile("" : "+s"(p)); return p; }
; __device__ __forceinline__ int tidx(int wid) { int l; asm volatile("v_mbcnt_lo_u32_b32 %0, -1, 0\n\tv_mbcnt_hi_u32_b32 %0, -1, %0" : "=v"(l)); return (wid << 6) + l; }
; __device__ __forceinline__ unsigned xb_ld(unsigned* p)              { return __hip_atomic_load(p, __ATOMIC_RELAXED, __HIP_MEMORY_SCOPE_AGENT); }
; __device__ __forceinline__ unsigned xb_add(unsigned* p, unsigned v) { return __hip_atomic_fetch_add(p, v, __ATOMIC_RELAXED, __HIP_MEMORY_SCOPE_AGENT); }
; #define XB_SPIN(cond, bar) do { unsigned _sp = 0; while (cond) { __builtin_amdgcn_s_sleep(1); \
;     if ((++_sp & 255u) == 0u) { if (xb_ld(&(bar)[XB_TMO])) break; if (_sp > XB_SPIN_CAP) { atomicAdd(&(bar)[XB_TMO], 1u); break; } } } } while (0)
; __device__ __forceinline__ void xcd_barrier(const XcdBarrier& b, int wid0) {
;     asm volatile("s_waitcnt vmcnt(0)" ::: "memory");
;     __syncthreads();
;     if (tidx(wid0) == 0) {
;         unsigned* bar = opaque_p(b.bar);
;         __builtin_amdgcn_s_waitcnt(0);
;         unsigned nloc = b.st[0], nx = b.st[1];
;         if (nloc == 0u) { xcd_barrier_complete(bar, b.x, nloc, nx); b.st[0] = nloc; b.st[1] = nx; }
;         const unsigned old = xb_add(&bar[XB_XSUB(b.x)], 1u);
;         const unsigned gen = old / nloc;
;         if (old + 1u == (gen + 1u) * nloc) {
;             __builtin_amdgcn_fence(__ATOMIC_RELEASE, "agent");
;             asm volatile("s_waitcnt vmcnt(0)" ::: "memory");
;             const unsigned og = xb_add(&bar[XB_TOP], 1u);
;             const unsigned tg = og / nx;
;             if (og + 1u == (tg + 1u) * nx) xb_add(&bar[XB_TOPGEN], 1u);
;             else XB_SPIN(xb_ld(&bar[XB_TOPGEN]) == tg, bar);
;             (void)xb_add(&bar[XB_XGEN(b.x)], 1u);
;             __builtin_amdgcn_fence(__ATOMIC_ACQUIRE, "agent");
;             asm volatile("s_waitcnt vmcnt(0)" ::: "memory");
;         } else {
;             XB_SPIN(xb_ld(&bar[XB_XGEN(b.x)]) == gen, bar);
;             __builtin_amdgcn_fence(__ATOMIC_ACQUIRE, "agent");
;             asm volatile("s_waitcnt vmcnt(0)" ::: "memory");
;         }
;     }
;     __syncthreads();
; }
.LBB0_284:
	s_or_b32 s36, s77, 2
	s_cmp_ge_i32 s36, s61
	s_cbranch_scc1 .LBB0_330
	s_waitcnt vmcnt(0)
	s_waitcnt vmcnt(0) lgkmcnt(0)
	s_barrier
	v_mbcnt_lo_u32_b32 v0, -1, 0
	v_mbcnt_hi_u32_b32 v0, -1, v0
	s_nop 0
	v_cmp_eq_u32_e32 vcc, s86, v0
	s_and_saveexec_b64 s[30:31], vcc
	s_cbranch_execz .LBB0_329
	v_readlane_b32 s34, v255, 3
	v_readlane_b32 s0, v255, 17
	v_readlane_b32 s35, v255, 4
	v_readlane_b32 s1, v255, 18
	s_lshl_b32 s2, s91, 2
	s_add_u32 s2, s34, s2
	s_addc_u32 s3, s35, 0
	s_add_u32 s4, s2, 0x1400
	s_addc_u32 s5, s3, 0
	s_add_u32 s6, s34, 0x3400
	s_addc_u32 s7, s35, 0
	v_mov_b32_e32 v0, s0
	v_mov_b32_e32 v1, s1
	ds_read_b32 v2, v0
	ds_read_b32 v12, v1
	v_mov_b32_e32 v6, 1
	v_mov_b32_e32 v8, s4
	v_mov_b32_e32 v9, s5
	v_mov_b32_e32 v10, s6
	v_mov_b32_e32 v11, s7
	s_nop 0
	global_atomic_add v3, v[8:9], v6, off sc0
	buffer_inv sc1
	s_waitcnt lgkmcnt(0)
	v_cvt_f32_u32_e32 v1, v2
	v_sub_u32_e32 v4, 0, v2
	v_rcp_iflag_f32_e32 v1, v1
	s_nop 0
	v_mul_f32_e32 v1, 0x4f7ffffe, v1
	v_cvt_u32_f32_e32 v1, v1
	v_mul_lo_u32 v4, v4, v1
	v_mul_hi_u32 v4, v1, v4
	v_add_u32_e32 v1, v1, v4
	s_mov_b32 s8, 0
	s_waitcnt vmcnt(0)
	v_mul_hi_u32 v1, v3, v1
	v_mul_lo_u32 v4, v1, v2
	v_sub_u32_e32 v4, v3, v4
	v_cmp_ge_u32_e32 vcc, v4, v2
	v_add_u32_e32 v5, 1, v1
	s_nop 1
	v_cndmask_b32_e32 v1, v1, v5, vcc
	v_sub_u32_e32 v5, v4, v2
	v_cndmask_b32_e32 v4, v4, v5, vcc
	v_cmp_ge_u32_e32 vcc, v4, v2
	v_add_u32_e32 v4, 1, v1
	s_nop 1
	v_cndmask_b32_e32 v1, v1, v4, vcc
	v_add_u32_e32 v1, 1, v1
	v_add_u32_e32 v4, 1, v3
	v_mul_lo_u32 v7, v1, v2
	v_mul_lo_u32 v13, v1, v12
	v_cmp_ne_u32_e32 vcc, v4, v7
	s_nop 1
	s_cbranch_vccnz .Lxb0_poll
	buffer_wbl2 sc1
	s_waitcnt vmcnt(0)
	global_atomic_add v[10:11], v6, off
.Lxb0_poll:
	global_load_dword v14, v[10:11], off sc1
	s_add_i32 s8, s8, 1
	s_waitcnt vmcnt(0)
	v_cmp_lt_u32_e32 vcc, v14, v13
	s_nop 1
	s_cbranch_vccz .Lxb0_done
	s_cmp_lt_u32 s8, 0x40000
	s_cbranch_scc0 .Lxb0_done
	s_sleep 1
	s_branch .Lxb0_poll
.Lxb0_done:
.LBB0_329:
	s_or_b64 exec, exec, s[30:31]
	s_barrier

; template <class T> __device__ __forceinline__ T* opaque_p(T* p) { asm volatile("" : "+s"(p)); return p; }
; __device__ __forceinline__ int tidx(int wid) { int l; asm volatile("v_mbcnt_lo_u32_b32 %0, -1, 0\n\tv_mbcnt_hi_u32_b32 %0, -1, %0" : "=v"(l)); return (wid << 6) + l; }
; __device__ __forceinline__ unsigned xb_ld(unsigned* p)              { return __hip_atomic_load(p, __ATOMIC_RELAXED, __HIP_MEMORY_SCOPE_AGENT); }
; __device__ __forceinline__ unsigned xb_add(unsigned* p, unsigned v) { return __hip_atomic_fetch_add(p, v, __ATOMIC_RELAXED, __HIP_MEMORY_SCOPE_AGENT); }
; #define XB_SPIN(cond, bar) do { unsigned _sp = 0; while (cond) { __builtin_amdgcn_s_sleep(1); \
;     if ((++_sp & 255u) == 0u) { if (xb_ld(&(bar)[XB_TMO])) break; if (_sp > XB_SPIN_CAP) { atomicAdd(&(bar)[XB_TMO], 1u); break; } } } } while (0)
; __device__ __forceinline__ void xcd_barrier(const XcdBarrier& b, int wid0) {
;     asm volatile("s_waitcnt vmcnt(0)" ::: "memory");
;     __syncthreads();
;     if (tidx(wid0) == 0) {
;         unsigned* bar = opaque_p(b.bar);
;         __builtin_amdgcn_s_waitcnt(0);
;         unsigned nloc = b.st[0], nx = b.st[1];
;         if (nloc == 0u) { xcd_barrier_complete(bar, b.x, nloc, nx); b.st[0] = nloc; b.st[1] = nx; }
;         const unsigned old = xb_add(&bar[XB_XSUB(b.x)], 1u);
;         const unsigned gen = old / nloc;
;         if (old + 1u == (gen + 1u) * nloc) {
;             __builtin_amdgcn_fence(__ATOMIC_RELEASE, "agent");
;             asm volatile("s_waitcnt vmcnt(0)" ::: "memory");
;             const unsigned og = xb_add(&bar[XB_TOP], 1u);
;             const unsigned tg = og / nx;
;             if (og + 1u == (tg + 1u) * nx) xb_add(&bar[XB_TOPGEN], 1u);
;             else XB_SPIN(xb_ld(&bar[XB_TOPGEN]) == tg, bar);
;             (void)xb_add(&bar[XB_XGEN(b.x)], 1u);
;             __builtin_amdgcn_fence(__ATOMIC_ACQUIRE, "agent");
;             asm volatile("s_waitcnt vmcnt(0)" ::: "memory");
;         } else {
;             XB_SPIN(xb_ld(&bar[XB_XGEN(b.x)]) == gen, bar);
;             __builtin_amdgcn_fence(__ATOMIC_ACQUIRE, "agent");
;             asm volatile("s_waitcnt vmcnt(0)" ::: "memory");
;         }
.LBB0_521:
	s_or_b32 s36, s77, 3
	s_cmp_lt_i32 s36, s61
	s_cbranch_scc0 .LBB0_567
	s_waitcnt vmcnt(0)
	s_barrier
	v_mbcnt_lo_u32_b32 v0, -1, 0
	v_mbcnt_hi_u32_b32 v0, -1, v0
	s_nop 0
	v_cmp_eq_u32_e32 vcc, s86, v0
	s_and_saveexec_b64 s[30:31], vcc
	s_cbranch_execz .LBB0_566
	v_readlane_b32 s34, v255, 3
	v_readlane_b32 s0, v255, 17
	v_readlane_b32 s35, v255, 4
	v_readlane_b32 s1, v255, 18
	s_lshl_b32 s2, s91, 2
	s_add_u32 s2, s34, s2
	s_addc_u32 s3, s35, 0
	s_add_u32 s4, s2, 0x1400
	s_addc_u32 s5, s3, 0
	s_add_u32 s6, s34, 0x3400
	s_addc_u32 s7, s35, 0
	v_mov_b32_e32 v0, s0
	v_mov_b32_e32 v1, s1
	ds_read_b32 v2, v0
	ds_read_b32 v12, v1
	v_mov_b32_e32 v6, 1
	v_mov_b32_e32 v8, s4
	v_mov_b32_e32 v9, s5
	v_mov_b32_e32 v10, s6
	v_mov_b32_e32 v11, s7
	s_nop 0
	global_atomic_add v3, v[8:9], v6, off sc0
	buffer_inv sc1
	s_waitcnt lgkmcnt(0)
	v_cvt_f32_u32_e32 v1, v2
	v_sub_u32_e32 v4, 0, v2
	v_rcp_iflag_f32_e32 v1, v1
	s_nop 0
	v_mul_f32_e32 v1, 0x4f7ffffe, v1
	v_cvt_u32_f32_e32 v1, v1
	v_mul_lo_u32 v4, v4, v1
	v_mul_hi_u32 v4, v1, v4
	v_add_u32_e32 v1, v1, v4
	s_mov_b32 s8, 0
	s_waitcnt vmcnt(0)
	v_mul_hi_u32 v1, v3, v1
	v_mul_lo_u32 v4, v1, v2
	v_sub_u32_e32 v4, v3, v4
	v_cmp_ge_u32_e32 vcc, v4, v2
	v_add_u32_e32 v5, 1, v1
	s_nop 1
	v_cndmask_b32_e32 v1, v1, v5, vcc
	v_sub_u32_e32 v5, v4, v2
	v_cndmask_b32_e32 v4, v4, v5, vcc
	v_cmp_ge_u32_e32 vcc, v4, v2
	v_add_u32_e32 v4, 1, v1
	s_nop 1
	v_cndmask_b32_e32 v1, v1, v4, vcc
	v_add_u32_e32 v1, 1, v1
	v_add_u32_e32 v4, 1, v3
	v_mul_lo_u32 v7, v1, v2
	v_mul_lo_u32 v13, v1, v12
	v_cmp_ne_u32_e32 vcc, v4, v7
	s_nop 1
	s_cbranch_vccnz .Lxb1_poll
	buffer_wbl2 sc1
	s_waitcnt vmcnt(0)
	global_atomic_add v[10:11], v6, off
.Lxb1_poll:
	global_load_dword v14, v[10:11], off sc1
	s_add_i32 s8, s8, 1
	s_waitcnt vmcnt(0)
	v_cmp_lt_u32_e32 vcc, v14, v13
	s_nop 1
	s_cbranch_vccz .Lxb1_done
	s_cmp_lt_u32 s8, 0x40000
	s_cbranch_scc0 .Lxb1_done
	s_sleep 1
	s_branch .Lxb1_poll
.Lxb1_done:
.LBB0_566:
	s_or_b64 exec, exec, s[30:31]
	s_barrier

; template <class T> __device__ __forceinline__ T* opaque_p(T* p) { asm volatile("" : "+s"(p)); return p; }
; __device__ __forceinline__ int tidx(int wid) { int l; asm volatile("v_mbcnt_lo_u32_b32 %0, -1, 0\n\tv_mbcnt_hi_u32_b32 %0, -1, %0" : "=v"(l)); return (wid << 6) + l; }
; __device__ __forceinline__ unsigned xb_ld(unsigned* p)              { return __hip_atomic_load(p, __ATOMIC_RELAXED, __HIP_MEMORY_SCOPE_AGENT); }
; __device__ __forceinline__ unsigned xb_add(unsigned* p, unsigned v) { return __hip_atomic_fetch_add(p, v, __ATOMIC_RELAXED, __HIP_MEMORY_SCOPE_AGENT); }
; #define XB_SPIN(cond, bar) do { unsigned _sp = 0; while (cond) { __builtin_amdgcn_s_sleep(1); \
;     if ((++_sp & 255u) == 0u) { if (xb_ld(&(bar)[XB_TMO])) break; if (_sp > XB_SPIN_CAP) { atomicAdd(&(bar)[XB_TMO], 1u); break; } } } } while (0)
; __device__ __forceinline__ void xcd_barrier(const XcdBarrier& b, int wid0) {
;     asm volatile("s_waitcnt vmcnt(0)" ::: "memory");
;     __syncthreads();
;     if (tidx(wid0) == 0) {
;         unsigned* bar = opaque_p(b.bar);
;         __builtin_amdgcn_s_waitcnt(0);
;         unsigned nloc = b.st[0], nx = b.st[1];
;         if (nloc == 0u) { xcd_barrier_complete(bar, b.x, nloc, nx); b.st[0] = nloc; b.st[1] = nx; }
;         const unsigned old = xb_add(&bar[XB_XSUB(b.x)], 1u);
;         const unsigned gen = old / nloc;
;         if (old + 1u == (gen + 1u) * nloc) {
;             __builtin_amdgcn_fence(__ATOMIC_RELEASE, "agent");
;             asm volatile("s_waitcnt vmcnt(0)" ::: "memory");
;             const unsigned og = xb_add(&bar[XB_TOP], 1u);
;             const unsigned tg = og / nx;
;             if (og + 1u == (tg + 1u) * nx) xb_add(&bar[XB_TOPGEN], 1u);
;             else XB_SPIN(xb_ld(&bar[XB_TOPGEN]) == tg, bar);
;             (void)xb_add(&bar[XB_XGEN(b.x)], 1u);
;             __builtin_amdgcn_fence(__ATOMIC_ACQUIRE, "agent");
;             asm volatile("s_waitcnt vmcnt(0)" ::: "memory");
;         } else {
;             XB_SPIN(xb_ld(&bar[XB_XGEN(b.x)]) == gen, bar);
;             __builtin_amdgcn_fence(__ATOMIC_ACQUIRE, "agent");
;             asm volatile("s_waitcnt vmcnt(0)" ::: "memory");
;         }
.LBB0_698:
	s_add_i32 s0, s77, 4
	s_cmp_ge_i32 s0, s61
	s_cbranch_scc1 .LBB0_744
	s_waitcnt vmcnt(0)
	s_waitcnt vmcnt(0) lgkmcnt(0)
	s_barrier
	v_mbcnt_lo_u32_b32 v0, -1, 0
	v_mbcnt_hi_u32_b32 v0, -1, v0
	s_nop 0
	v_cmp_eq_u32_e32 vcc, s86, v0
	s_and_saveexec_b64 s[30:31], vcc
	s_cbranch_execz .LBB0_743
	v_readlane_b32 s34, v255, 3
	v_readlane_b32 s0, v255, 17
	v_readlane_b32 s35, v255, 4
	v_readlane_b32 s1, v255, 18
	s_lshl_b32 s2, s91, 2
	s_add_u32 s2, s34, s2
	s_addc_u32 s3, s35, 0
	s_add_u32 s4, s2, 0x1400
	s_addc_u32 s5, s3, 0
	s_add_u32 s6, s34, 0x3400
	s_addc_u32 s7, s35, 0
	v_mov_b32_e32 v0, s0
	v_mov_b32_e32 v1, s1
	ds_read_b32 v2, v0
	ds_read_b32 v12, v1
	v_mov_b32_e32 v6, 1
	v_mov_b32_e32 v8, s4
	v_mov_b32_e32 v9, s5
	v_mov_b32_e32 v10, s6
	v_mov_b32_e32 v11, s7
	s_nop 0
	global_atomic_add v3, v[8:9], v6, off sc0
	buffer_inv sc1
	s_waitcnt lgkmcnt(0)
	v_cvt_f32_u32_e32 v1, v2
	v_sub_u32_e32 v4, 0, v2
	v_rcp_iflag_f32_e32 v1, v1
	s_nop 0
	v_mul_f32_e32 v1, 0x4f7ffffe, v1
	v_cvt_u32_f32_e32 v1, v1
	v_mul_lo_u32 v4, v4, v1
	v_mul_hi_u32 v4, v1, v4
	v_add_u32_e32 v1, v1, v4
	s_mov_b32 s8, 0
	s_waitcnt vmcnt(0)
	v_mul_hi_u32 v1, v3, v1
	v_mul_lo_u32 v4, v1, v2
	v_sub_u32_e32 v4, v3, v4
	v_cmp_ge_u32_e32 vcc, v4, v2
	v_add_u32_e32 v5, 1, v1
	s_nop 1
	v_cndmask_b32_e32 v1, v1, v5, vcc
	v_sub_u32_e32 v5, v4, v2
	v_cndmask_b32_e32 v4, v4, v5, vcc
	v_cmp_ge_u32_e32 vcc, v4, v2
	v_add_u32_e32 v4, 1, v1
	s_nop 1
	v_cndmask_b32_e32 v1, v1, v4, vcc
	v_add_u32_e32 v1, 1, v1
	v_add_u32_e32 v4, 1, v3
	v_mul_lo_u32 v7, v1, v2
	v_mul_lo_u32 v13, v1, v12
	v_cmp_ne_u32_e32 vcc, v4, v7
	s_nop 1
	s_cbranch_vccnz .Lxb2_poll
	buffer_wbl2 sc1
	s_waitcnt vmcnt(0)
	global_atomic_add v[10:11], v6, off
.Lxb2_poll:
	global_load_dword v14, v[10:11], off sc1
	s_add_i32 s8, s8, 1
	s_waitcnt vmcnt(0)
	v_cmp_lt_u32_e32 vcc, v14, v13
	s_nop 1
	s_cbranch_vccz .Lxb2_done
	s_cmp_lt_u32 s8, 0x40000
	s_cbranch_scc0 .Lxb2_done
	s_sleep 1
	s_branch .Lxb2_poll
.Lxb2_done:
.LBB0_743:
	s_or_b64 exec, exec, s[30:31]
	s_barrier

; template <class T> __device__ __forceinline__ T* opaque_p(T* p) { asm volatile("" : "+s"(p)); return p; }
; __device__ __forceinline__ int tidx(int wid) { int l; asm volatile("v_mbcnt_lo_u32_b32 %0, -1, 0\n\tv_mbcnt_hi_u32_b32 %0, -1, %0" : "=v"(l)); return (wid << 6) + l; }
; __device__ __forceinline__ unsigned xb_ld(unsigned* p)              { return __hip_atomic_load(p, __ATOMIC_RELAXED, __HIP_MEMORY_SCOPE_AGENT); }
; __device__ __forceinline__ unsigned xb_add(unsigned* p, unsigned v) { return __hip_atomic_fetch_add(p, v, __ATOMIC_RELAXED, __HIP_MEMORY_SCOPE_AGENT); }
; #define XB_SPIN(cond, bar) do { unsigned _sp = 0; while (cond) { __builtin_amdgcn_s_sleep(1); \
;     if ((++_sp & 255u) == 0u) { if (xb_ld(&(bar)[XB_TMO])) break; if (_sp > XB_SPIN_CAP) { atomicAdd(&(bar)[XB_TMO], 1u); break; } } } } while (0)
; __device__ __forceinline__ void xcd_barrier(const XcdBarrier& b, int wid0) {
;     asm volatile("s_waitcnt vmcnt(0)" ::: "memory");
;     __syncthreads();
;     if (tidx(wid0) == 0) {
;         unsigned* bar = opaque_p(b.bar);
;         __builtin_amdgcn_s_waitcnt(0);
;         unsigned nloc = b.st[0], nx = b.st[1];
;         if (nloc == 0u) { xcd_barrier_complete(bar, b.x, nloc, nx); b.st[0] = nloc; b.st[1] = nx; }
;         const unsigned old = xb_add(&bar[XB_XSUB(b.x)], 1u);
;         const unsigned gen = old / nloc;
;         if (old + 1u == (gen + 1u) * nloc) {
;             __builtin_amdgcn_fence(__ATOMIC_RELEASE, "agent");
;             asm volatile("s_waitcnt vmcnt(0)" ::: "memory");
;             const unsigned og = xb_add(&bar[XB_TOP], 1u);
;             const unsigned tg = og / nx;
;             if (og + 1u == (tg + 1u) * nx) xb_add(&bar[XB_TOPGEN], 1u);
;             else XB_SPIN(xb_ld(&bar[XB_TOPGEN]) == tg, bar);
;             (void)xb_add(&bar[XB_XGEN(b.x)], 1u);
;             __builtin_amdgcn_fence(__ATOMIC_ACQUIRE, "agent");
;             asm volatile("s_waitcnt vmcnt(0)" ::: "memory");
;         } else {
;             XB_SPIN(xb_ld(&bar[XB_XGEN(b.x)]) == gen, bar);
;             __builtin_amdgcn_fence(__ATOMIC_ACQUIRE, "agent");
;             asm volatile("s_waitcnt vmcnt(0)" ::: "memory");
;         }
.LBB0_759:
	v_readlane_b32 s0, v255, 33
	s_add_i32 s36, s77, 6
	v_readlane_b32 s1, v255, 34
	s_cmp_lt_i32 s36, s1
	s_cbranch_scc0 .LBB0_772
	s_waitcnt vmcnt(0)
	s_waitcnt lgkmcnt(0)
	s_barrier
	v_mbcnt_lo_u32_b32 v0, -1, 0
	v_mbcnt_hi_u32_b32 v0, -1, v0
	s_nop 0
	v_cmp_eq_u32_e32 vcc, s86, v0
	s_and_saveexec_b64 s[30:31], vcc
	s_mov_b32 s93, s61
	v_readlane_b32 s96, v255, 28
	v_readlane_b32 s60, v255, 33
	v_readlane_b32 s97, v255, 29
	v_readlane_b32 s94, v255, 32
	v_readlane_b32 s61, v255, 34
	s_cbranch_execz .LBB0_805
	v_readlane_b32 s34, v255, 3
	v_readlane_b32 s0, v255, 17
	v_readlane_b32 s35, v255, 4
	v_readlane_b32 s1, v255, 18
	s_lshl_b32 s2, s91, 2
	s_add_u32 s2, s34, s2
	s_addc_u32 s3, s35, 0
	s_add_u32 s4, s2, 0x1400
	s_addc_u32 s5, s3, 0
	s_add_u32 s6, s34, 0x3400
	s_addc_u32 s7, s35, 0
	v_mov_b32_e32 v0, s0
	v_mov_b32_e32 v1, s1
	ds_read_b32 v2, v0
	ds_read_b32 v12, v1
	v_mov_b32_e32 v6, 1
	v_mov_b32_e32 v8, s4
	v_mov_b32_e32 v9, s5
	v_mov_b32_e32 v10, s6
	v_mov_b32_e32 v11, s7
	s_nop 0
	global_atomic_add v3, v[8:9], v6, off sc0
	buffer_inv sc1
	s_waitcnt lgkmcnt(0)
	v_cvt_f32_u32_e32 v1, v2
	v_sub_u32_e32 v4, 0, v2
	v_rcp_iflag_f32_e32 v1, v1
	s_nop 0
	v_mul_f32_e32 v1, 0x4f7ffffe, v1
	v_cvt_u32_f32_e32 v1, v1
	v_mul_lo_u32 v4, v4, v1
	v_mul_hi_u32 v4, v1, v4
	v_add_u32_e32 v1, v1, v4
	s_mov_b32 s8, 0
	s_waitcnt vmcnt(0)
	v_mul_hi_u32 v1, v3, v1
	v_mul_lo_u32 v4, v1, v2
	v_sub_u32_e32 v4, v3, v4
	v_cmp_ge_u32_e32 vcc, v4, v2
	v_add_u32_e32 v5, 1, v1
	s_nop 1
	v_cndmask_b32_e32 v1, v1, v5, vcc
	v_sub_u32_e32 v5, v4, v2
	v_cndmask_b32_e32 v4, v4, v5, vcc
	v_cmp_ge_u32_e32 vcc, v4, v2
	v_add_u32_e32 v4, 1, v1
	s_nop 1
	v_cndmask_b32_e32 v1, v1, v4, vcc
	v_add_u32_e32 v1, 1, v1
	v_add_u32_e32 v4, 1, v3
	v_mul_lo_u32 v7, v1, v2
	v_mul_lo_u32 v13, v1, v12
	v_cmp_ne_u32_e32 vcc, v4, v7
	s_nop 1
	s_cbranch_vccnz .Lxb3_poll
	buffer_wbl2 sc1
	s_waitcnt vmcnt(0)
	global_atomic_add v[10:11], v6, off
.Lxb3_poll:
	global_load_dword v14, v[10:11], off sc1
	s_add_i32 s8, s8, 1
	s_waitcnt vmcnt(0)
	v_cmp_lt_u32_e32 vcc, v14, v13
	s_nop 1
	s_cbranch_vccz .Lxb3_done
	s_cmp_lt_u32 s8, 0x40000
	s_cbranch_scc0 .Lxb3_done
	s_sleep 1
	s_branch .Lxb3_poll
.Lxb3_done:
	s_branch .LBB0_805

; template <class T> __device__ __forceinline__ T* opaque_p(T* p) { asm volatile("" : "+s"(p)); return p; }
; __device__ __forceinline__ int tidx(int wid) { int l; asm volatile("v_mbcnt_lo_u32_b32 %0, -1, 0\n\tv_mbcnt_hi_u32_b32 %0, -1, %0" : "=v"(l)); return (wid << 6) + l; }
; __device__ __forceinline__ unsigned xb_ld(unsigned* p)              { return __hip_atomic_load(p, __ATOMIC_RELAXED, __HIP_MEMORY_SCOPE_AGENT); }
; __device__ __forceinline__ unsigned xb_add(unsigned* p, unsigned v) { return __hip_atomic_fetch_add(p, v, __ATOMIC_RELAXED, __HIP_MEMORY_SCOPE_AGENT); }
; #define XB_SPIN(cond, bar) do { unsigned _sp = 0; while (cond) { __builtin_amdgcn_s_sleep(1); \
;     if ((++_sp & 255u) == 0u) { if (xb_ld(&(bar)[XB_TMO])) break; if (_sp > XB_SPIN_CAP) { atomicAdd(&(bar)[XB_TMO], 1u); break; } } } } while (0)
; __device__ __forceinline__ void xcd_barrier(const XcdBarrier& b, int wid0) {
;     asm volatile("s_waitcnt vmcnt(0)" ::: "memory");
;     __syncthreads();
;     if (tidx(wid0) == 0) {
;         unsigned* bar = opaque_p(b.bar);
;         __builtin_amdgcn_s_waitcnt(0);
;         unsigned nloc = b.st[0], nx = b.st[1];
;         if (nloc == 0u) { xcd_barrier_complete(bar, b.x, nloc, nx); b.st[0] = nloc; b.st[1] = nx; }
;         const unsigned old = xb_add(&bar[XB_XSUB(b.x)], 1u);
;         const unsigned gen = old / nloc;
;         if (old + 1u == (gen + 1u) * nloc) {
;             __builtin_amdgcn_fence(__ATOMIC_RELEASE, "agent");
;             asm volatile("s_waitcnt vmcnt(0)" ::: "memory");
;             const unsigned og = xb_add(&bar[XB_TOP], 1u);
;             const unsigned tg = og / nx;
;             if (og + 1u == (tg + 1u) * nx) xb_add(&bar[XB_TOPGEN], 1u);
;             else XB_SPIN(xb_ld(&bar[XB_TOPGEN]) == tg, bar);
;             (void)xb_add(&bar[XB_XGEN(b.x)], 1u);
;             __builtin_amdgcn_fence(__ATOMIC_ACQUIRE, "agent");
;             asm volatile("s_waitcnt vmcnt(0)" ::: "memory");
;         } else {
;             XB_SPIN(xb_ld(&bar[XB_XGEN(b.x)]) == gen, bar);
;             __builtin_amdgcn_fence(__ATOMIC_ACQUIRE, "agent");
;             asm volatile("s_waitcnt vmcnt(0)" ::: "memory");
;         }
.LBB0_835:
	s_add_i32 s36, s77, 7
	s_cmp_ge_i32 s36, s61
	s_cbranch_scc1 .LBB0_881
	s_waitcnt vmcnt(0)
	s_waitcnt lgkmcnt(0)
	s_barrier
	v_mbcnt_lo_u32_b32 v0, -1, 0
	v_mbcnt_hi_u32_b32 v0, -1, v0
	s_nop 0
	v_cmp_eq_u32_e32 vcc, s86, v0
	s_and_saveexec_b64 s[30:31], vcc
	s_cbranch_execz .LBB0_880
	v_readlane_b32 s34, v255, 3
	v_readlane_b32 s0, v255, 17
	v_readlane_b32 s35, v255, 4
	v_readlane_b32 s1, v255, 18
	s_lshl_b32 s2, s91, 2
	s_add_u32 s2, s34, s2
	s_addc_u32 s3, s35, 0
	s_add_u32 s4, s2, 0x1400
	s_addc_u32 s5, s3, 0
	s_add_u32 s6, s34, 0x3400
	s_addc_u32 s7, s35, 0
	v_mov_b32_e32 v0, s0
	v_mov_b32_e32 v1, s1
	ds_read_b32 v2, v0
	ds_read_b32 v12, v1
	v_mov_b32_e32 v6, 1
	v_mov_b32_e32 v8, s4
	v_mov_b32_e32 v9, s5
	v_mov_b32_e32 v10, s6
	v_mov_b32_e32 v11, s7
	s_nop 0
	global_atomic_add v3, v[8:9], v6, off sc0
	buffer_inv sc1
	s_waitcnt lgkmcnt(0)
	v_cvt_f32_u32_e32 v1, v2
	v_sub_u32_e32 v4, 0, v2
	v_rcp_iflag_f32_e32 v1, v1
	s_nop 0
	v_mul_f32_e32 v1, 0x4f7ffffe, v1
	v_cvt_u32_f32_e32 v1, v1
	v_mul_lo_u32 v4, v4, v1
	v_mul_hi_u32 v4, v1, v4
	v_add_u32_e32 v1, v1, v4
	s_mov_b32 s8, 0
	s_waitcnt vmcnt(0)
	v_mul_hi_u32 v1, v3, v1
	v_mul_lo_u32 v4, v1, v2
	v_sub_u32_e32 v4, v3, v4
	v_cmp_ge_u32_e32 vcc, v4, v2
	v_add_u32_e32 v5, 1, v1
	s_nop 1
	v_cndmask_b32_e32 v1, v1, v5, vcc
	v_sub_u32_e32 v5, v4, v2
	v_cndmask_b32_e32 v4, v4, v5, vcc
	v_cmp_ge_u32_e32 vcc, v4, v2
	v_add_u32_e32 v4, 1, v1
	s_nop 1
	v_cndmask_b32_e32 v1, v1, v4, vcc
	v_add_u32_e32 v1, 1, v1
	v_add_u32_e32 v4, 1, v3
	v_mul_lo_u32 v7, v1, v2
	v_mul_lo_u32 v13, v1, v12
	v_cmp_ne_u32_e32 vcc, v4, v7
	s_nop 1
	s_cbranch_vccnz .Lxb4_poll
	buffer_wbl2 sc1
	s_waitcnt vmcnt(0)
	global_atomic_add v[10:11], v6, off
.Lxb4_poll:
	global_load_dword v14, v[10:11], off sc1
	s_add_i32 s8, s8, 1
	s_waitcnt vmcnt(0)
	v_cmp_lt_u32_e32 vcc, v14, v13
	s_nop 1
	s_cbranch_vccz .Lxb4_done
	s_cmp_lt_u32 s8, 0x40000
	s_cbranch_scc0 .Lxb4_done
	s_sleep 1
	s_branch .Lxb4_poll
.Lxb4_done:
.LBB0_880:
	s_or_b64 exec, exec, s[30:31]
	s_barrier

; template <class T> __device__ __forceinline__ T* opaque_p(T* p) { asm volatile("" : "+s"(p)); return p; }
; __device__ __forceinline__ int tidx(int wid) { int l; asm volatile("v_mbcnt_lo_u32_b32 %0, -1, 0\n\tv_mbcnt_hi_u32_b32 %0, -1, %0" : "=v"(l)); return (wid << 6) + l; }
; __device__ __forceinline__ unsigned xb_ld(unsigned* p)              { return __hip_atomic_load(p, __ATOMIC_RELAXED, __HIP_MEMORY_SCOPE_AGENT); }
; __device__ __forceinline__ unsigned xb_add(unsigned* p, unsigned v) { return __hip_atomic_fetch_add(p, v, __ATOMIC_RELAXED, __HIP_MEMORY_SCOPE_AGENT); }
; #define XB_SPIN(cond, bar) do { unsigned _sp = 0; while (cond) { __builtin_amdgcn_s_sleep(1); \
;     if ((++_sp & 255u) == 0u) { if (xb_ld(&(bar)[XB_TMO])) break; if (_sp > XB_SPIN_CAP) { atomicAdd(&(bar)[XB_TMO], 1u); break; } } } } while (0)
; __device__ __forceinline__ void xcd_barrier(const XcdBarrier& b, int wid0) {
;     asm volatile("s_waitcnt vmcnt(0)" ::: "memory");
;     __syncthreads();
;     if (tidx(wid0) == 0) {
;         unsigned* bar = opaque_p(b.bar);
;         __builtin_amdgcn_s_waitcnt(0);
;         unsigned nloc = b.st[0], nx = b.st[1];
;         if (nloc == 0u) { xcd_barrier_complete(bar, b.x, nloc, nx); b.st[0] = nloc; b.st[1] = nx; }
;         const unsigned old = xb_add(&bar[XB_XSUB(b.x)], 1u);
;         const unsigned gen = old / nloc;
;         if (old + 1u == (gen + 1u) * nloc) {
;             __builtin_amdgcn_fence(__ATOMIC_RELEASE, "agent");
;             asm volatile("s_waitcnt vmcnt(0)" ::: "memory");
;             const unsigned og = xb_add(&bar[XB_TOP], 1u);
;             const unsigned tg = og / nx;
;             if (og + 1u == (tg + 1u) * nx) xb_add(&bar[XB_TOPGEN], 1u);
;             else XB_SPIN(xb_ld(&bar[XB_TOPGEN]) == tg, bar);
;             (void)xb_add(&bar[XB_XGEN(b.x)], 1u);
;             __builtin_amdgcn_fence(__ATOMIC_ACQUIRE, "agent");
;             asm volatile("s_waitcnt vmcnt(0)" ::: "memory");
;         } else {
;             XB_SPIN(xb_ld(&bar[XB_XGEN(b.x)]) == gen, bar);
;             __builtin_amdgcn_fence(__ATOMIC_ACQUIRE, "agent");
;             asm volatile("s_waitcnt vmcnt(0)" ::: "memory");
;         }
.LBB0_934:
	s_add_i32 s0, s77, 8
	s_cmp_lt_i32 s0, s61
	s_cselect_b64 s[0:1], -1, 0
	s_and_b64 s[0:1], s[20:21], s[0:1]
	s_andn2_b64 vcc, exec, s[0:1]
	s_cbranch_vccnz .LBB0_980
	s_waitcnt vmcnt(0)
	s_waitcnt vmcnt(0) lgkmcnt(0)
	s_barrier
	v_mbcnt_lo_u32_b32 v0, -1, 0
	v_mbcnt_hi_u32_b32 v0, -1, v0
	s_nop 0
	v_cmp_eq_u32_e32 vcc, s86, v0
	s_and_saveexec_b64 s[30:31], vcc
	s_cbranch_execz .LBB0_979
	v_readlane_b32 s34, v255, 3
	v_readlane_b32 s0, v255, 17
	v_readlane_b32 s35, v255, 4
	v_readlane_b32 s1, v255, 18
	s_lshl_b32 s2, s91, 2
	s_add_u32 s2, s34, s2
	s_addc_u32 s3, s35, 0
	s_add_u32 s4, s2, 0x1400
	s_addc_u32 s5, s3, 0
	s_add_u32 s6, s34, 0x3400
	s_addc_u32 s7, s35, 0
	v_mov_b32_e32 v0, s0
	v_mov_b32_e32 v1, s1
	ds_read_b32 v2, v0
	ds_read_b32 v12, v1
	v_mov_b32_e32 v6, 1
	v_mov_b32_e32 v8, s4
	v_mov_b32_e32 v9, s5
	v_mov_b32_e32 v10, s6
	v_mov_b32_e32 v11, s7
	s_nop 0
	global_atomic_add v3, v[8:9], v6, off sc0
	buffer_inv sc1
	s_waitcnt lgkmcnt(0)
	v_cvt_f32_u32_e32 v1, v2
	v_sub_u32_e32 v4, 0, v2
	v_rcp_iflag_f32_e32 v1, v1
	s_nop 0
	v_mul_f32_e32 v1, 0x4f7ffffe, v1
	v_cvt_u32_f32_e32 v1, v1
	v_mul_lo_u32 v4, v4, v1
	v_mul_hi_u32 v4, v1, v4
	v_add_u32_e32 v1, v1, v4
	s_mov_b32 s8, 0
	s_waitcnt vmcnt(0)
	v_mul_hi_u32 v1, v3, v1
	v_mul_lo_u32 v4, v1, v2
	v_sub_u32_e32 v4, v3, v4
	v_cmp_ge_u32_e32 vcc, v4, v2
	v_add_u32_e32 v5, 1, v1
	s_nop 1
	v_cndmask_b32_e32 v1, v1, v5, vcc
	v_sub_u32_e32 v5, v4, v2
	v_cndmask_b32_e32 v4, v4, v5, vcc
	v_cmp_ge_u32_e32 vcc, v4, v2
	v_add_u32_e32 v4, 1, v1
	s_nop 1
	v_cndmask_b32_e32 v1, v1, v4, vcc
	v_add_u32_e32 v1, 1, v1
	v_add_u32_e32 v4, 1, v3
	v_mul_lo_u32 v7, v1, v2
	v_mul_lo_u32 v13, v1, v12
	v_cmp_ne_u32_e32 vcc, v4, v7
	s_nop 1
	s_cbranch_vccnz .Lxb5_poll
	buffer_wbl2 sc1
	s_waitcnt vmcnt(0)
	global_atomic_add v[10:11], v6, off
.Lxb5_poll:
	global_load_dword v14, v[10:11], off sc1
	s_add_i32 s8, s8, 1
	s_waitcnt vmcnt(0)
	v_cmp_lt_u32_e32 vcc, v14, v13
	s_nop 1
	s_cbranch_vccz .Lxb5_done
	s_cmp_lt_u32 s8, 0x40000
	s_cbranch_scc0 .Lxb5_done
	s_sleep 1
	s_branch .Lxb5_poll
.Lxb5_done:
.LBB0_979:
	s_or_b64 exec, exec, s[30:31]
	s_barrier

; template <class T> __device__ __forceinline__ T* opaque_p(T* p) { asm volatile("" : "+s"(p)); return p; }
; __device__ __forceinline__ int tidx(int wid) { int l; asm volatile("v_mbcnt_lo_u32_b32 %0, -1, 0\n\tv_mbcnt_hi_u32_b32 %0, -1, %0" : "=v"(l)); return (wid << 6) + l; }
; __device__ __forceinline__ unsigned xb_ld(unsigned* p)              { return __hip_atomic_load(p, __ATOMIC_RELAXED, __HIP_MEMORY_SCOPE_AGENT); }
; __device__ __forceinline__ unsigned xb_add(unsigned* p, unsigned v) { return __hip_atomic_fetch_add(p, v, __ATOMIC_RELAXED, __HIP_MEMORY_SCOPE_AGENT); }
; #define XB_SPIN(cond, bar) do { unsigned _sp = 0; while (cond) { __builtin_amdgcn_s_sleep(1); \
;     if ((++_sp & 255u) == 0u) { if (xb_ld(&(bar)[XB_TMO])) break; if (_sp > XB_SPIN_CAP) { atomicAdd(&(bar)[XB_TMO], 1u); break; } } } } while (0)
; __device__ __forceinline__ void xcd_barrier(const XcdBarrier& b, int wid0) {
;     asm volatile("s_waitcnt vmcnt(0)" ::: "memory");
;     __syncthreads();
;     if (tidx(wid0) == 0) {
;         unsigned* bar = opaque_p(b.bar);
;         __builtin_amdgcn_s_waitcnt(0);
;         unsigned nloc = b.st[0], nx = b.st[1];
;         if (nloc == 0u) { xcd_barrier_complete(bar, b.x, nloc, nx); b.st[0] = nloc; b.st[1] = nx; }
;         const unsigned old = xb_add(&bar[XB_XSUB(b.x)], 1u);
;         const unsigned gen = old / nloc;
;         if (old + 1u == (gen + 1u) * nloc) {
;             __builtin_amdgcn_fence(__ATOMIC_RELEASE, "agent");
;             asm volatile("s_waitcnt vmcnt(0)" ::: "memory");
;             const unsigned og = xb_add(&bar[XB_TOP], 1u);
;             const unsigned tg = og / nx;
;             if (og + 1u == (tg + 1u) * nx) xb_add(&bar[XB_TOPGEN], 1u);
;             else XB_SPIN(xb_ld(&bar[XB_TOPGEN]) == tg, bar);
;             (void)xb_add(&bar[XB_XGEN(b.x)], 1u);
;             __builtin_amdgcn_fence(__ATOMIC_ACQUIRE, "agent");
;             asm volatile("s_waitcnt vmcnt(0)" ::: "memory");
;         } else {
;             XB_SPIN(xb_ld(&bar[XB_XGEN(b.x)]) == gen, bar);
;             __builtin_amdgcn_fence(__ATOMIC_ACQUIRE, "agent");
;             asm volatile("s_waitcnt vmcnt(0)" ::: "memory");
;         }
.LBB0_1033:
	s_waitcnt vmcnt(0)
	s_waitcnt vmcnt(0) lgkmcnt(0)
	s_barrier
	v_mbcnt_lo_u32_b32 v0, -1, 0
	v_mbcnt_hi_u32_b32 v0, -1, v0
	s_nop 0
	v_cmp_eq_u32_e32 vcc, s86, v0
	s_and_saveexec_b64 s[30:31], vcc
	s_cbranch_execz .LBB0_1077
	v_readlane_b32 s34, v255, 3
	v_readlane_b32 s0, v255, 17
	v_readlane_b32 s35, v255, 4
	v_readlane_b32 s1, v255, 18
	s_lshl_b32 s2, s91, 2
	s_add_u32 s2, s34, s2
	s_addc_u32 s3, s35, 0
	s_add_u32 s4, s2, 0x1400
	s_addc_u32 s5, s3, 0
	s_add_u32 s6, s34, 0x3400
	s_addc_u32 s7, s35, 0
	v_mov_b32_e32 v0, s0
	v_mov_b32_e32 v1, s1
	ds_read_b32 v2, v0
	ds_read_b32 v12, v1
	v_mov_b32_e32 v6, 1
	v_mov_b32_e32 v8, s4
	v_mov_b32_e32 v9, s5
	v_mov_b32_e32 v10, s6
	v_mov_b32_e32 v11, s7
	s_nop 0
	global_atomic_add v3, v[8:9], v6, off sc0
	buffer_inv sc1
	s_waitcnt lgkmcnt(0)
	v_cvt_f32_u32_e32 v1, v2
	v_sub_u32_e32 v4, 0, v2
	v_rcp_iflag_f32_e32 v1, v1
	s_nop 0
	v_mul_f32_e32 v1, 0x4f7ffffe, v1
	v_cvt_u32_f32_e32 v1, v1
	v_mul_lo_u32 v4, v4, v1
	v_mul_hi_u32 v4, v1, v4
	v_add_u32_e32 v1, v1, v4
	s_mov_b32 s8, 0
	s_waitcnt vmcnt(0)
	v_mul_hi_u32 v1, v3, v1
	v_mul_lo_u32 v4, v1, v2
	v_sub_u32_e32 v4, v3, v4
	v_cmp_ge_u32_e32 vcc, v4, v2
	v_add_u32_e32 v5, 1, v1
	s_nop 1
	v_cndmask_b32_e32 v1, v1, v5, vcc
	v_sub_u32_e32 v5, v4, v2
	v_cndmask_b32_e32 v4, v4, v5, vcc
	v_cmp_ge_u32_e32 vcc, v4, v2
	v_add_u32_e32 v4, 1, v1
	s_nop 1
	v_cndmask_b32_e32 v1, v1, v4, vcc
	v_add_u32_e32 v1, 1, v1
	v_add_u32_e32 v4, 1, v3
	v_mul_lo_u32 v7, v1, v2
	v_mul_lo_u32 v13, v1, v12
	v_cmp_ne_u32_e32 vcc, v4, v7
	s_nop 1
	s_cbranch_vccnz .Lxb6_poll
	buffer_wbl2 sc1
	s_waitcnt vmcnt(0)
	global_atomic_add v[10:11], v6, off
.Lxb6_poll:
	global_load_dword v14, v[10:11], off sc1
	s_add_i32 s8, s8, 1
	s_waitcnt vmcnt(0)
	v_cmp_lt_u32_e32 vcc, v14, v13
	s_nop 1
	s_cbranch_vccz .Lxb6_done
	s_cmp_lt_u32 s8, 0x40000
	s_cbranch_scc0 .Lxb6_done
	s_sleep 1
	s_branch .Lxb6_poll
.Lxb6_done:
.LBB0_1077:
	s_or_b64 exec, exec, s[30:31]
	s_barrier

; template <class T> __device__ __forceinline__ T* opaque_p(T* p) { asm volatile("" : "+s"(p)); return p; }
; __device__ __forceinline__ int tidx(int wid) { int l; asm volatile("v_mbcnt_lo_u32_b32 %0, -1, 0\n\tv_mbcnt_hi_u32_b32 %0, -1, %0" : "=v"(l)); return (wid << 6) + l; }
; __device__ __forceinline__ unsigned xb_ld(unsigned* p)              { return __hip_atomic_load(p, __ATOMIC_RELAXED, __HIP_MEMORY_SCOPE_AGENT); }
; __device__ __forceinline__ unsigned xb_add(unsigned* p, unsigned v) { return __hip_atomic_fetch_add(p, v, __ATOMIC_RELAXED, __HIP_MEMORY_SCOPE_AGENT); }
; #define XB_SPIN(cond, bar) do { unsigned _sp = 0; while (cond) { __builtin_amdgcn_s_sleep(1); \
;     if ((++_sp & 255u) == 0u) { if (xb_ld(&(bar)[XB_TMO])) break; if (_sp > XB_SPIN_CAP) { atomicAdd(&(bar)[XB_TMO], 1u); break; } } } } while (0)
; __device__ __forceinline__ void xcd_barrier(const XcdBarrier& b, int wid0) {
;     asm volatile("s_waitcnt vmcnt(0)" ::: "memory");
;     __syncthreads();
;     if (tidx(wid0) == 0) {
;         unsigned* bar = opaque_p(b.bar);
;         __builtin_amdgcn_s_waitcnt(0);
;         unsigned nloc = b.st[0], nx = b.st[1];
;         if (nloc == 0u) { xcd_barrier_complete(bar, b.x, nloc, nx); b.st[0] = nloc; b.st[1] = nx; }
;         const unsigned old = xb_add(&bar[XB_XSUB(b.x)], 1u);
;         const unsigned gen = old / nloc;
;         if (old + 1u == (gen + 1u) * nloc) {
;             __builtin_amdgcn_fence(__ATOMIC_RELEASE, "agent");
;             asm volatile("s_waitcnt vmcnt(0)" ::: "memory");
;             const unsigned og = xb_add(&bar[XB_TOP], 1u);
;             const unsigned tg = og / nx;
;             if (og + 1u == (tg + 1u) * nx) xb_add(&bar[XB_TOPGEN], 1u);
;             else XB_SPIN(xb_ld(&bar[XB_TOPGEN]) == tg, bar);
;             (void)xb_add(&bar[XB_XGEN(b.x)], 1u);
;             __builtin_amdgcn_fence(__ATOMIC_ACQUIRE, "agent");
;             asm volatile("s_waitcnt vmcnt(0)" ::: "memory");
;         } else {
;             XB_SPIN(xb_ld(&bar[XB_XGEN(b.x)]) == gen, bar);
;             __builtin_amdgcn_fence(__ATOMIC_ACQUIRE, "agent");
;             asm volatile("s_waitcnt vmcnt(0)" ::: "memory");
;         }
.LBB0_1145:
	s_add_i32 s36, s77, 11
	s_cmp_ge_i32 s36, s61
	s_cbranch_scc1 .LBB0_1191
	s_waitcnt vmcnt(0)
	s_waitcnt vmcnt(0) lgkmcnt(0)
	s_barrier
	v_mbcnt_lo_u32_b32 v0, -1, 0
	v_mbcnt_hi_u32_b32 v0, -1, v0
	s_nop 0
	v_cmp_eq_u32_e32 vcc, s86, v0
	s_and_saveexec_b64 s[30:31], vcc
	s_cbranch_execz .LBB0_1190
	v_readlane_b32 s34, v255, 3
	v_readlane_b32 s0, v255, 17
	v_readlane_b32 s35, v255, 4
	v_readlane_b32 s1, v255, 18
	s_lshl_b32 s2, s91, 2
	s_add_u32 s2, s34, s2
	s_addc_u32 s3, s35, 0
	s_add_u32 s4, s2, 0x1400
	s_addc_u32 s5, s3, 0
	s_add_u32 s6, s34, 0x3400
	s_addc_u32 s7, s35, 0
	v_mov_b32_e32 v0, s0
	v_mov_b32_e32 v1, s1
	ds_read_b32 v2, v0
	ds_read_b32 v12, v1
	v_mov_b32_e32 v6, 1
	v_mov_b32_e32 v8, s4
	v_mov_b32_e32 v9, s5
	v_mov_b32_e32 v10, s6
	v_mov_b32_e32 v11, s7
	s_nop 0
	global_atomic_add v3, v[8:9], v6, off sc0
	buffer_inv sc1
	s_waitcnt lgkmcnt(0)
	v_cvt_f32_u32_e32 v1, v2
	v_sub_u32_e32 v4, 0, v2
	v_rcp_iflag_f32_e32 v1, v1
	s_nop 0
	v_mul_f32_e32 v1, 0x4f7ffffe, v1
	v_cvt_u32_f32_e32 v1, v1
	v_mul_lo_u32 v4, v4, v1
	v_mul_hi_u32 v4, v1, v4
	v_add_u32_e32 v1, v1, v4
	s_mov_b32 s8, 0
	s_waitcnt vmcnt(0)
	v_mul_hi_u32 v1, v3, v1
	v_mul_lo_u32 v4, v1, v2
	v_sub_u32_e32 v4, v3, v4
	v_cmp_ge_u32_e32 vcc, v4, v2
	v_add_u32_e32 v5, 1, v1
	s_nop 1
	v_cndmask_b32_e32 v1, v1, v5, vcc
	v_sub_u32_e32 v5, v4, v2
	v_cndmask_b32_e32 v4, v4, v5, vcc
	v_cmp_ge_u32_e32 vcc, v4, v2
	v_add_u32_e32 v4, 1, v1
	s_nop 1
	v_cndmask_b32_e32 v1, v1, v4, vcc
	v_add_u32_e32 v1, 1, v1
	v_add_u32_e32 v4, 1, v3
	v_mul_lo_u32 v7, v1, v2
	v_mul_lo_u32 v13, v1, v12
	v_cmp_ne_u32_e32 vcc, v4, v7
	s_nop 1
	s_cbranch_vccnz .Lxb7_poll
	buffer_wbl2 sc1
	s_waitcnt vmcnt(0)
	global_atomic_add v[10:11], v6, off
.Lxb7_poll:
	global_load_dword v14, v[10:11], off sc1
	s_add_i32 s8, s8, 1
	s_waitcnt vmcnt(0)
	v_cmp_lt_u32_e32 vcc, v14, v13
	s_nop 1
	s_cbranch_vccz .Lxb7_done
	s_cmp_lt_u32 s8, 0x40000
	s_cbranch_scc0 .Lxb7_done
	s_sleep 1
	s_branch .Lxb7_poll
.Lxb7_done:
.LBB0_1190:
	s_or_b64 exec, exec, s[30:31]
	s_barrier

; template <class T> __device__ __forceinline__ T* opaque_p(T* p) { asm volatile("" : "+s"(p)); return p; }
; __device__ __forceinline__ int tidx(int wid) { int l; asm volatile("v_mbcnt_lo_u32_b32 %0, -1, 0\n\tv_mbcnt_hi_u32_b32 %0, -1, %0" : "=v"(l)); return (wid << 6) + l; }
; __device__ __forceinline__ unsigned xb_ld(unsigned* p)              { return __hip_atomic_load(p, __ATOMIC_RELAXED, __HIP_MEMORY_SCOPE_AGENT); }
; __device__ __forceinline__ unsigned xb_add(unsigned* p, unsigned v) { return __hip_atomic_fetch_add(p, v, __ATOMIC_RELAXED, __HIP_MEMORY_SCOPE_AGENT); }
; #define XB_SPIN(cond, bar) do { unsigned _sp = 0; while (cond) { __builtin_amdgcn_s_sleep(1); \
;     if ((++_sp & 255u) == 0u) { if (xb_ld(&(bar)[XB_TMO])) break; if (_sp > XB_SPIN_CAP) { atomicAdd(&(bar)[XB_TMO], 1u); break; } } } } while (0)
; __device__ __forceinline__ void xcd_barrier(const XcdBarrier& b, int wid0) {
;     asm volatile("s_waitcnt vmcnt(0)" ::: "memory");
;     __syncthreads();
;     if (tidx(wid0) == 0) {
;         unsigned* bar = opaque_p(b.bar);
;         __builtin_amdgcn_s_waitcnt(0);
;         unsigned nloc = b.st[0], nx = b.st[1];
;         if (nloc == 0u) { xcd_barrier_complete(bar, b.x, nloc, nx); b.st[0] = nloc; b.st[1] = nx; }
;         const unsigned old = xb_add(&bar[XB_XSUB(b.x)], 1u);
;         const unsigned gen = old / nloc;
;         if (old + 1u == (gen + 1u) * nloc) {
;             __builtin_amdgcn_fence(__ATOMIC_RELEASE, "agent");
;             asm volatile("s_waitcnt vmcnt(0)" ::: "memory");
;             const unsigned og = xb_add(&bar[XB_TOP], 1u);
;             const unsigned tg = og / nx;
;             if (og + 1u == (tg + 1u) * nx) xb_add(&bar[XB_TOPGEN], 1u);
;             else XB_SPIN(xb_ld(&bar[XB_TOPGEN]) == tg, bar);
;             (void)xb_add(&bar[XB_XGEN(b.x)], 1u);
;             __builtin_amdgcn_fence(__ATOMIC_ACQUIRE, "agent");
;             asm volatile("s_waitcnt vmcnt(0)" ::: "memory");
;         } else {
;             XB_SPIN(xb_ld(&bar[XB_XGEN(b.x)]) == gen, bar);
;             __builtin_amdgcn_fence(__ATOMIC_ACQUIRE, "agent");
;             asm volatile("s_waitcnt vmcnt(0)" ::: "memory");
;         }
.LBB0_1284:
	s_add_i32 s36, s77, 12
	s_cmp_ge_i32 s36, s61
	s_cbranch_scc1 .LBB0_1330
	s_waitcnt vmcnt(0)
	s_waitcnt lgkmcnt(0)
	s_barrier
	s_waitcnt vmcnt(0)
	v_mbcnt_lo_u32_b32 v0, -1, 0
	v_mbcnt_hi_u32_b32 v0, -1, v0
	s_nop 0
	v_cmp_eq_u32_e32 vcc, s86, v0
	s_and_saveexec_b64 s[30:31], vcc
	s_cbranch_execz .LBB0_1329
	v_readlane_b32 s34, v255, 3
	v_readlane_b32 s0, v255, 17
	v_readlane_b32 s35, v255, 4
	v_readlane_b32 s1, v255, 18
	s_lshl_b32 s2, s91, 2
	s_add_u32 s2, s34, s2
	s_addc_u32 s3, s35, 0
	s_add_u32 s4, s2, 0x1400
	s_addc_u32 s5, s3, 0
	s_add_u32 s6, s34, 0x3400
	s_addc_u32 s7, s35, 0
	v_mov_b32_e32 v0, s0
	v_mov_b32_e32 v1, s1
	ds_read_b32 v2, v0
	ds_read_b32 v12, v1
	v_mov_b32_e32 v6, 1
	v_mov_b32_e32 v8, s4
	v_mov_b32_e32 v9, s5
	v_mov_b32_e32 v10, s6
	v_mov_b32_e32 v11, s7
	s_nop 0
	global_atomic_add v3, v[8:9], v6, off sc0
	buffer_inv sc1
	s_waitcnt lgkmcnt(0)
	v_cvt_f32_u32_e32 v1, v2
	v_sub_u32_e32 v4, 0, v2
	v_rcp_iflag_f32_e32 v1, v1
	s_nop 0
	v_mul_f32_e32 v1, 0x4f7ffffe, v1
	v_cvt_u32_f32_e32 v1, v1
	v_mul_lo_u32 v4, v4, v1
	v_mul_hi_u32 v4, v1, v4
	v_add_u32_e32 v1, v1, v4
	s_mov_b32 s8, 0
	s_waitcnt vmcnt(0)
	v_mul_hi_u32 v1, v3, v1
	v_mul_lo_u32 v4, v1, v2
	v_sub_u32_e32 v4, v3, v4
	v_cmp_ge_u32_e32 vcc, v4, v2
	v_add_u32_e32 v5, 1, v1
	s_nop 1
	v_cndmask_b32_e32 v1, v1, v5, vcc
	v_sub_u32_e32 v5, v4, v2
	v_cndmask_b32_e32 v4, v4, v5, vcc
	v_cmp_ge_u32_e32 vcc, v4, v2
	v_add_u32_e32 v4, 1, v1
	s_nop 1
	v_cndmask_b32_e32 v1, v1, v4, vcc
	v_add_u32_e32 v1, 1, v1
	v_add_u32_e32 v4, 1, v3
	v_mul_lo_u32 v7, v1, v2
	v_mul_lo_u32 v13, v1, v12
	v_cmp_ne_u32_e32 vcc, v4, v7
	s_nop 1
	s_cbranch_vccnz .Lxb8_poll
	buffer_wbl2 sc1
	s_waitcnt vmcnt(0)
	global_atomic_add v[10:11], v6, off
.Lxb8_poll:
	global_load_dword v14, v[10:11], off sc1
	s_add_i32 s8, s8, 1
	s_waitcnt vmcnt(0)
	v_cmp_lt_u32_e32 vcc, v14, v13
	s_nop 1
	s_cbranch_vccz .Lxb8_done
	s_cmp_lt_u32 s8, 0x40000
	s_cbranch_scc0 .Lxb8_done
	s_sleep 1
	s_branch .Lxb8_poll
.Lxb8_done:
.LBB0_1329:
	s_or_b64 exec, exec, s[30:31]
	s_barrier

; template <class T> __device__ __forceinline__ T* opaque_p(T* p) { asm volatile("" : "+s"(p)); return p; }
; __device__ __forceinline__ int tidx(int wid) { int l; asm volatile("v_mbcnt_lo_u32_b32 %0, -1, 0\n\tv_mbcnt_hi_u32_b32 %0, -1, %0" : "=v"(l)); return (wid << 6) + l; }
; __device__ __forceinline__ unsigned xb_ld(unsigned* p)              { return __hip_atomic_load(p, __ATOMIC_RELAXED, __HIP_MEMORY_SCOPE_AGENT); }
; __device__ __forceinline__ unsigned xb_add(unsigned* p, unsigned v) { return __hip_atomic_fetch_add(p, v, __ATOMIC_RELAXED, __HIP_MEMORY_SCOPE_AGENT); }
; #define XB_SPIN(cond, bar) do { unsigned _sp = 0; while (cond) { __builtin_amdgcn_s_sleep(1); \
;     if ((++_sp & 255u) == 0u) { if (xb_ld(&(bar)[XB_TMO])) break; if (_sp > XB_SPIN_CAP) { atomicAdd(&(bar)[XB_TMO], 1u); break; } } } } while (0)
; __device__ __forceinline__ void xcd_barrier(const XcdBarrier& b, int wid0) {
;     asm volatile("s_waitcnt vmcnt(0)" ::: "memory");
;     __syncthreads();
;     if (tidx(wid0) == 0) {
;         unsigned* bar = opaque_p(b.bar);
;         __builtin_amdgcn_s_waitcnt(0);
;         unsigned nloc = b.st[0], nx = b.st[1];
;         if (nloc == 0u) { xcd_barrier_complete(bar, b.x, nloc, nx); b.st[0] = nloc; b.st[1] = nx; }
;         const unsigned old = xb_add(&bar[XB_XSUB(b.x)], 1u);
;         const unsigned gen = old / nloc;
;         if (old + 1u == (gen + 1u) * nloc) {
;             __builtin_amdgcn_fence(__ATOMIC_RELEASE, "agent");
;             asm volatile("s_waitcnt vmcnt(0)" ::: "memory");
;             const unsigned og = xb_add(&bar[XB_TOP], 1u);
;             const unsigned tg = og / nx;
;             if (og + 1u == (tg + 1u) * nx) xb_add(&bar[XB_TOPGEN], 1u);
;             else XB_SPIN(xb_ld(&bar[XB_TOPGEN]) == tg, bar);
;             (void)xb_add(&bar[XB_XGEN(b.x)], 1u);
;             __builtin_amdgcn_fence(__ATOMIC_ACQUIRE, "agent");
;             asm volatile("s_waitcnt vmcnt(0)" ::: "memory");
;         } else {
;             XB_SPIN(xb_ld(&bar[XB_XGEN(b.x)]) == gen, bar);
;             __builtin_amdgcn_fence(__ATOMIC_ACQUIRE, "agent");
;             asm volatile("s_waitcnt vmcnt(0)" ::: "memory");
;         }
.LBB0_1507:
	v_readlane_b32 s34, v255, 3
	v_readlane_b32 s0, v255, 17
	v_readlane_b32 s35, v255, 4
	v_readlane_b32 s1, v255, 18
	s_lshl_b32 s2, s91, 2
	s_add_u32 s2, s34, s2
	s_addc_u32 s3, s35, 0
	s_add_u32 s4, s2, 0x1400
	s_addc_u32 s5, s3, 0
	s_add_u32 s6, s34, 0x3400
	s_addc_u32 s7, s35, 0
	v_mov_b32_e32 v0, s0
	v_mov_b32_e32 v1, s1
	ds_read_b32 v2, v0
	ds_read_b32 v12, v1
	v_mov_b32_e32 v6, 1
	v_mov_b32_e32 v8, s4
	v_mov_b32_e32 v9, s5
	v_mov_b32_e32 v10, s6
	v_mov_b32_e32 v11, s7
	s_nop 0
	global_atomic_add v3, v[8:9], v6, off sc0
	buffer_inv sc1
	s_waitcnt lgkmcnt(0)
	v_cvt_f32_u32_e32 v1, v2
	v_sub_u32_e32 v4, 0, v2
	v_rcp_iflag_f32_e32 v1, v1
	s_nop 0
	v_mul_f32_e32 v1, 0x4f7ffffe, v1
	v_cvt_u32_f32_e32 v1, v1
	v_mul_lo_u32 v4, v4, v1
	v_mul_hi_u32 v4, v1, v4
	v_add_u32_e32 v1, v1, v4
	s_mov_b32 s8, 0
	s_waitcnt vmcnt(0)
	v_mul_hi_u32 v1, v3, v1
	v_mul_lo_u32 v4, v1, v2
	v_sub_u32_e32 v4, v3, v4
	v_cmp_ge_u32_e32 vcc, v4, v2
	v_add_u32_e32 v5, 1, v1
	s_nop 1
	v_cndmask_b32_e32 v1, v1, v5, vcc
	v_sub_u32_e32 v5, v4, v2
	v_cndmask_b32_e32 v4, v4, v5, vcc
	v_cmp_ge_u32_e32 vcc, v4, v2
	v_add_u32_e32 v4, 1, v1
	s_nop 1
	v_cndmask_b32_e32 v1, v1, v4, vcc
	v_add_u32_e32 v1, 1, v1
	v_add_u32_e32 v4, 1, v3
	v_mul_lo_u32 v7, v1, v2
	v_mul_lo_u32 v13, v1, v12
	v_cmp_ne_u32_e32 vcc, v4, v7
	s_nop 1
	s_cbranch_vccnz .Lxb9_poll
	buffer_wbl2 sc1
	s_waitcnt vmcnt(0)
	global_atomic_add v[10:11], v6, off
.Lxb9_poll:
	global_load_dword v14, v[10:11], off sc1
	s_add_i32 s8, s8, 1
	s_waitcnt vmcnt(0)
	v_cmp_lt_u32_e32 vcc, v14, v13
	s_nop 1
	s_cbranch_vccz .Lxb9_done
	s_cmp_lt_u32 s8, 0x40000
	s_cbranch_scc0 .Lxb9_done
	s_sleep 1
	s_branch .Lxb9_poll
.Lxb9_done:
	s_branch .Lxb9_out
